# v69 variant: plain tiles (8,9) moved to the last round (the critical workgroups' fifth unit), sigmoid tiles shifted one round earlier
# baseline (speedup 1.0000x reference)
;     __device__ bool next(int i, Unit& u) const { if (!base.next(i >> 1, u)) return false; if (i & 1) { u.pm += MTOK / BM; u.pn += DM / BM; } return true; }
;   __device__ __forceinline__ bool next(int i,AttnUnit&u)const{ if(i>=2||vcu>=256)return false; const int s=vcu&3; u.bh=vcu>>2; u.qb=(i==0)?7-s:s; return true; }
;     __host__ __device__ bool next(int i, Unit& u) const {
;         const int L = i * G + c; if (L >= nwg) return false;
;         int wgid = L; { const int q = nwg / NXCD, r = nwg % NXCD, xcd = wgid % NXCD, off = wgid / NXCD; wgid = (xcd < r ? xcd * (q + 1) : r * (q + 1) + (xcd - r) * q) + off; }
;         const int nig = WGM * nN, gid = wgid / nig, fm = gid * WGM, gsz = (nM - fm) < WGM ? (nM - fm) : WGM;
;         u.pm = fm + ((wgid % nig) % gsz); u.pn = (wgid % nig) / gsz; u.half = 0; return true;
.LBB0_382:
	s_ashr_i32 s4, s21, 31
	s_lshr_b32 s4, s4, 29
	s_add_i32 s4, s21, s4
	s_ashr_i32 s5, s4, 3
	s_and_b32 s4, s4, -8
	s_sub_i32 s4, s21, s4
	s_cmp_lt_i32 s4, 0
	s_movk_i32 s6, 0x91
	s_cselect_b32 s6, s6, 0x90
	s_mul_i32 s4, s4, s6
	s_add_i32 s4, s4, s5
	s_mul_hi_i32 s5, s4, 0x38e38e39
	s_lshr_b32 s6, s5, 31
	s_ashr_i32 s5, s5, 5
	s_add_i32 s5, s5, s6
	s_lshl_b32 s6, s5, 3
	s_mulk_i32 s5, 0x90
	s_sub_i32 s4, s4, s5
	s_bfe_u32 s5, s4, 0x3001c
	s_add_i32 s5, s4, s5
	s_sext_i32_i16 s7, s5
	s_and_b32 s5, s5, 0xfff8
	s_sub_i32 s4, s4, s5
	s_sext_i32_i16 s4, s4
	s_add_i32 s18, s6, s4
	s_ashr_i32 s70, s7, 3
	s_mul_i32 s4, s70, 5
	s_cmp_lt_u32 s70, 12
	s_cbranch_scc0 .Lpn_hi0
	s_mov_b32 s6, 0x86229020
	s_mov_b32 s7, 0x6b16a39
	s_branch .Lpn_go0
.Lpn_hi0:
	s_sub_i32 s4, s4, 60
	s_mov_b32 s6, 0x1288c1ee
	s_mov_b32 s7, 0

;     __device__ bool next(int i, Unit& u) const { if (!base.next(i >> 1, u)) return false; if (i & 1) { u.pm += MTOK / BM; u.pn += DM / BM; } return true; }
;   __device__ __forceinline__ bool next(int i,AttnUnit&u)const{ if(i>=2||vcu>=256)return false; const int s=vcu&3; u.bh=vcu>>2; u.qb=(i==0)?7-s:s; return true; }
;     __host__ __device__ bool next(int i, Unit& u) const {
;         const int L = i * G + c; if (L >= nwg) return false;
;         int wgid = L; { const int q = nwg / NXCD, r = nwg % NXCD, xcd = wgid % NXCD, off = wgid / NXCD; wgid = (xcd < r ? xcd * (q + 1) : r * (q + 1) + (xcd - r) * q) + off; }
;         const int nig = WGM * nN, gid = wgid / nig, fm = gid * WGM, gsz = (nM - fm) < WGM ? (nM - fm) : WGM;
;         u.pm = fm + ((wgid % nig) % gsz); u.pn = (wgid % nig) / gsz; u.half = 0; return true;
; template <class Epi, class Sched, bool ALIGN_EPI = false, bool SP2 = false>
; __device__ __forceinline__ void gemm_phase(PG8_LAS unsigned char* lds, const Gemm g, const Sched& S, const Epi& E) {
;     ...
;         const bool has_next = S.next(ui + 1, nxt);
;         const char* nA = has_next ? (const char*)g.A + (size_t)nxt.pm * tstep + (nxt.half == 2 ? hstep : (size_t)0) : cA; const char* nB = has_next ? (const char*)g.Bt + (size_t)nxt.pn * tstep : cB;
.LBB0_392:
	s_add_i32 s72, s72, 1
	s_mul_i32 s10, s72, s33
	s_add_i32 s10, s10, s21
	s_cmpk_lt_i32 s10, 0x480
	s_cselect_b64 s[64:65], -1, 0
	s_cmpk_gt_i32 s10, 0x47f
	s_cbranch_scc1 .LBB0_394
	s_ashr_i32 s11, s10, 31
	s_lshr_b32 s11, s11, 29
	s_add_i32 s11, s10, s11
	s_ashr_i32 s12, s11, 3
	s_and_b32 s11, s11, -8
	s_sub_i32 s10, s10, s11
	s_cmp_lt_i32 s10, 0
	s_movk_i32 s11, 0x91
	s_cselect_b32 s11, s11, 0x90
	s_mul_i32 s10, s10, s11
	s_add_i32 s10, s10, s12
	s_mul_hi_i32 s11, s10, 0x38e38e39
	s_lshr_b32 s12, s11, 31
	s_ashr_i32 s11, s11, 5
	s_add_i32 s11, s11, s12
	s_lshl_b32 s12, s11, 3
	s_mulk_i32 s11, 0x90
	s_sub_i32 s10, s10, s11
	s_bfe_u32 s11, s10, 0x3001c
	s_add_i32 s11, s10, s11
	s_sext_i32_i16 s13, s11
	s_and_b32 s11, s11, 0xfff8
	s_sub_i32 s10, s10, s11
	s_sext_i32_i16 s10, s10
	s_add_i32 s60, s12, s10
	s_ashr_i32 s62, s13, 3
	s_mul_i32 s10, s62, 5
	s_cmp_lt_u32 s62, 12
	s_cbranch_scc0 .Lpn_hi1
	s_mov_b32 s12, 0x86229020
	s_mov_b32 s13, 0x6b16a39
	s_branch .Lpn_go1
.Lpn_hi1:
	s_sub_i32 s10, s10, 60
	s_mov_b32 s12, 0x1288c1ee
	s_mov_b32 s13, 0
